# P5/P15 router-weight*gain LDS fill: 64 loads per thread in flight instead of ~10 dependent load/wait/ds_write round trips
# speedup vs baseline: 1.0149x; 1.0007x over previous
; #define LAS __attribute__((address_space(3)))
; #define SEAM(k) do { if (IN(k) && IN((k) + 1)) GRID_BAR(); } while (0)
; __device__ __forceinline__ void norm_router_table(const float* g, const float* Wr, LAS float* WT, int tid) {
;     for (int idx = tid; idx < NE * DM; idx += NWAVES * 64) { const int e = idx & 15, d = idx >> 4; WT[e * WT_PITCH + ((d >> 3) & 3) * 256 + (d >> 5) * 8 + (d & 7)] = Wr[idx] * g[d]; }
; }
; __global__ void __launch_bounds__(NWAVES * 64, 2) enc_fwd(Args args) {
;     ...
;     { const bool fused_ = IN(4) && IN(5) && MK_SINGLE;
;     ...
;       if (fused_) { xcd_barrier_arrive(bar); norm_router_table(args.in[9], args.in[10], (LAS float*)lds, tid_k); xcd_barrier_wait(bar); }
;     ...
;       if (!fused_) SEAM(4);
;       rt_ready = fused_; }
.LBB0_528:
	v_readlane_b32 s4, v254, 12
	v_readlane_b32 s5, v254, 13
	s_cmp_lt_i32 s4, 6
	v_readlane_b32 s6, v254, 0
	s_cselect_b64 s[4:5], -1, 0
	v_readlane_b32 s7, v254, 1
	s_add_u32 s6, s6, 0xe00000
	s_addc_u32 s7, s7, 0
	s_and_b64 s[0:1], s[4:5], s[0:1]
	v_writelane_b32 v255, s6, 13
	v_cndmask_b32_e64 v1, 0, 1, s[0:1]
	v_cmp_ne_u32_e64 s[4:5], 1, v1
	v_writelane_b32 v255, s7, 14
	s_andn2_b64 vcc, exec, s[0:1]
	v_writelane_b32 v255, s4, 29
	s_nop 1
	v_writelane_b32 v255, s5, 30
	s_cbranch_vccnz .LBB0_550
	v_mov_b32_e32 v18, v0
	s_movk_i32 s4, 0x4000
	s_xor_b64 s[2:3], s[2:3], -1
	v_cmp_gt_i32_e32 vcc, s4, v18
	s_and_b64 s[4:5], s[2:3], vcc
	v_and_b32_e32 v1, 15, v18
	s_movk_i32 s2, 0x1010
	s_mov_b64 s[6:7], -1
	v_mad_u32_u24 v20, v1, s2, 0
	s_and_saveexec_b64 s[2:3], s[4:5]
	s_cbranch_execz .LBB0_541
; #define LAS __attribute__((address_space(3)))
; __device__ __forceinline__ void norm_router_table(const float* g, const float* Wr, LAS float* WT, int tid) {
;     for (int idx = tid; idx < NE * DM; idx += NWAVES * 64) { const int e = idx & 15, d = idx >> 4; WT[e * WT_PITCH + ((d >> 3) & 3) * 256 + (d >> 5) * 8 + (d & 7)] = Wr[idx] * g[d]; }
; }
	v_lshlrev_b32_e32 v21, 2, v18
	v_lshrrev_b32_e32 v22, 4, v18
	v_lshlrev_b32_e32 v23, 2, v22
	v_lshrrev_b32_e32 v24, 3, v22
	v_and_b32_e32 v25, 7, v22
	v_lshl_add_u32 v24, v24, 10, v20
	v_lshl_add_u32 v24, v25, 2, v24
	global_load_dword v30, v21, s[80:81]
	global_load_dword v31, v21, s[80:81] offset:2048
	s_add_u32 s8, s80, 0x1000
	s_addc_u32 s9, s81, 0
	global_load_dword v32, v21, s[8:9]
	global_load_dword v33, v21, s[8:9] offset:2048
	s_add_u32 s8, s80, 0x2000
	s_addc_u32 s9, s81, 0
	global_load_dword v34, v21, s[8:9]
	global_load_dword v35, v21, s[8:9] offset:2048
	s_add_u32 s8, s80, 0x3000
	s_addc_u32 s9, s81, 0
	global_load_dword v36, v21, s[8:9]
	global_load_dword v37, v21, s[8:9] offset:2048
	s_add_u32 s8, s80, 0x4000
	s_addc_u32 s9, s81, 0
	global_load_dword v38, v21, s[8:9]
	global_load_dword v39, v21, s[8:9] offset:2048
	s_add_u32 s8, s80, 0x5000
	s_addc_u32 s9, s81, 0
	global_load_dword v40, v21, s[8:9]
	global_load_dword v41, v21, s[8:9] offset:2048
	s_add_u32 s8, s80, 0x6000
	s_addc_u32 s9, s81, 0
	global_load_dword v42, v21, s[8:9]
	global_load_dword v43, v21, s[8:9] offset:2048
	s_add_u32 s8, s80, 0x7000
	s_addc_u32 s9, s81, 0
	global_load_dword v44, v21, s[8:9]
	global_load_dword v45, v21, s[8:9] offset:2048
	s_add_u32 s8, s80, 0x8000
	s_addc_u32 s9, s81, 0
	global_load_dword v46, v21, s[8:9]
	global_load_dword v47, v21, s[8:9] offset:2048
	s_add_u32 s8, s80, 0x9000
	s_addc_u32 s9, s81, 0
	global_load_dword v48, v21, s[8:9]
	global_load_dword v49, v21, s[8:9] offset:2048
	s_add_u32 s8, s80, 0xa000
	s_addc_u32 s9, s81, 0
	global_load_dword v50, v21, s[8:9]
	global_load_dword v51, v21, s[8:9] offset:2048
	s_add_u32 s8, s80, 0xb000
	s_addc_u32 s9, s81, 0
	global_load_dword v52, v21, s[8:9]
	global_load_dword v53, v21, s[8:9] offset:2048
	s_add_u32 s8, s80, 0xc000
	s_addc_u32 s9, s81, 0
	global_load_dword v54, v21, s[8:9]
	global_load_dword v55, v21, s[8:9] offset:2048
	s_add_u32 s8, s80, 0xd000
	s_addc_u32 s9, s81, 0
	global_load_dword v56, v21, s[8:9]
	global_load_dword v57, v21, s[8:9] offset:2048
	s_add_u32 s8, s80, 0xe000
	s_addc_u32 s9, s81, 0
	global_load_dword v58, v21, s[8:9]
	global_load_dword v59, v21, s[8:9] offset:2048
	s_add_u32 s8, s80, 0xf000
	s_addc_u32 s9, s81, 0
	global_load_dword v60, v21, s[8:9]
	global_load_dword v61, v21, s[8:9] offset:2048
	global_load_dword v62, v23, s[78:79]
	global_load_dword v63, v23, s[78:79] offset:128
	global_load_dword v64, v23, s[78:79] offset:256
	global_load_dword v65, v23, s[78:79] offset:384
	global_load_dword v66, v23, s[78:79] offset:512
	global_load_dword v67, v23, s[78:79] offset:640
	global_load_dword v68, v23, s[78:79] offset:768
	global_load_dword v69, v23, s[78:79] offset:896
	global_load_dword v70, v23, s[78:79] offset:1024
	global_load_dword v71, v23, s[78:79] offset:1152
	global_load_dword v72, v23, s[78:79] offset:1280
	global_load_dword v73, v23, s[78:79] offset:1408
	global_load_dword v74, v23, s[78:79] offset:1536
	global_load_dword v75, v23, s[78:79] offset:1664
	global_load_dword v76, v23, s[78:79] offset:1792
	global_load_dword v77, v23, s[78:79] offset:1920
	global_load_dword v78, v23, s[78:79] offset:2048
	global_load_dword v79, v23, s[78:79] offset:2176
	global_load_dword v80, v23, s[78:79] offset:2304
	global_load_dword v81, v23, s[78:79] offset:2432
	global_load_dword v82, v23, s[78:79] offset:2560
	global_load_dword v83, v23, s[78:79] offset:2688
	global_load_dword v84, v23, s[78:79] offset:2816
	global_load_dword v85, v23, s[78:79] offset:2944
	global_load_dword v86, v23, s[78:79] offset:3072
	global_load_dword v87, v23, s[78:79] offset:3200
	global_load_dword v88, v23, s[78:79] offset:3328
	global_load_dword v89, v23, s[78:79] offset:3456
	global_load_dword v90, v23, s[78:79] offset:3584
	global_load_dword v91, v23, s[78:79] offset:3712
	global_load_dword v92, v23, s[78:79] offset:3840
	global_load_dword v93, v23, s[78:79] offset:3968
	s_waitcnt vmcnt(31)
	v_mul_f32_e32 v30, v30, v62
	ds_write_b32 v24, v30
	s_waitcnt vmcnt(30)
	v_mul_f32_e32 v31, v31, v63
	ds_write_b32 v24, v31 offset:32
	s_waitcnt vmcnt(29)
	v_mul_f32_e32 v32, v32, v64
	ds_write_b32 v24, v32 offset:64
	s_waitcnt vmcnt(28)
	v_mul_f32_e32 v33, v33, v65
	ds_write_b32 v24, v33 offset:96
	s_waitcnt vmcnt(27)
	v_mul_f32_e32 v34, v34, v66
	ds_write_b32 v24, v34 offset:128
	s_waitcnt vmcnt(26)
	v_mul_f32_e32 v35, v35, v67
	ds_write_b32 v24, v35 offset:160
	s_waitcnt vmcnt(25)
	v_mul_f32_e32 v36, v36, v68
	ds_write_b32 v24, v36 offset:192
	s_waitcnt vmcnt(24)
	v_mul_f32_e32 v37, v37, v69
	ds_write_b32 v24, v37 offset:224
	s_waitcnt vmcnt(23)
	v_mul_f32_e32 v38, v38, v70
	ds_write_b32 v24, v38 offset:256
	s_waitcnt vmcnt(22)
	v_mul_f32_e32 v39, v39, v71
	ds_write_b32 v24, v39 offset:288
	s_waitcnt vmcnt(21)
	v_mul_f32_e32 v40, v40, v72
	ds_write_b32 v24, v40 offset:320
	s_waitcnt vmcnt(20)
	v_mul_f32_e32 v41, v41, v73
	ds_write_b32 v24, v41 offset:352
	s_waitcnt vmcnt(19)
	v_mul_f32_e32 v42, v42, v74
	ds_write_b32 v24, v42 offset:384
	s_waitcnt vmcnt(18)
	v_mul_f32_e32 v43, v43, v75
	ds_write_b32 v24, v43 offset:416
	s_waitcnt vmcnt(17)
	v_mul_f32_e32 v44, v44, v76
	ds_write_b32 v24, v44 offset:448
	s_waitcnt vmcnt(16)
	v_mul_f32_e32 v45, v45, v77
	ds_write_b32 v24, v45 offset:480
	s_waitcnt vmcnt(15)
	v_mul_f32_e32 v46, v46, v78
	ds_write_b32 v24, v46 offset:512
	s_waitcnt vmcnt(14)
	v_mul_f32_e32 v47, v47, v79
	ds_write_b32 v24, v47 offset:544
	s_waitcnt vmcnt(13)
	v_mul_f32_e32 v48, v48, v80
	ds_write_b32 v24, v48 offset:576
	s_waitcnt vmcnt(12)
	v_mul_f32_e32 v49, v49, v81
	ds_write_b32 v24, v49 offset:608
	s_waitcnt vmcnt(11)
	v_mul_f32_e32 v50, v50, v82
	ds_write_b32 v24, v50 offset:640
	s_waitcnt vmcnt(10)
	v_mul_f32_e32 v51, v51, v83
	ds_write_b32 v24, v51 offset:672
	s_waitcnt vmcnt(9)
	v_mul_f32_e32 v52, v52, v84
	ds_write_b32 v24, v52 offset:704
	s_waitcnt vmcnt(8)
	v_mul_f32_e32 v53, v53, v85
	ds_write_b32 v24, v53 offset:736
	s_waitcnt vmcnt(7)
	v_mul_f32_e32 v54, v54, v86
	ds_write_b32 v24, v54 offset:768
	s_waitcnt vmcnt(6)
	v_mul_f32_e32 v55, v55, v87
	ds_write_b32 v24, v55 offset:800
	s_waitcnt vmcnt(5)
	v_mul_f32_e32 v56, v56, v88
	ds_write_b32 v24, v56 offset:832
	s_waitcnt vmcnt(4)
	v_mul_f32_e32 v57, v57, v89
	ds_write_b32 v24, v57 offset:864
	s_waitcnt vmcnt(3)
	v_mul_f32_e32 v58, v58, v90
	ds_write_b32 v24, v58 offset:896
	s_waitcnt vmcnt(2)
	v_mul_f32_e32 v59, v59, v91
	ds_write_b32 v24, v59 offset:928
	s_waitcnt vmcnt(1)
	v_mul_f32_e32 v60, v60, v92
	ds_write_b32 v24, v60 offset:960
	s_waitcnt vmcnt(0)
	v_mul_f32_e32 v61, v61, v93
	ds_write_b32 v24, v61 offset:992

; #define LAS __attribute__((address_space(3)))
; #define SEAM(k) do { if (IN(k) && IN((k) + 1)) GRID_BAR(); } while (0)
; __device__ __forceinline__ void norm_router_table(const float* g, const float* Wr, LAS float* WT, int tid) {
;     for (int idx = tid; idx < NE * DM; idx += NWAVES * 64) { const int e = idx & 15, d = idx >> 4; WT[e * WT_PITCH + ((d >> 3) & 3) * 256 + (d >> 5) * 8 + (d & 7)] = Wr[idx] * g[d]; }
; }
; __global__ void __launch_bounds__(NWAVES * 64, 2) enc_fwd(Args args) {
;     ...
;     { const bool fused_ = IN(14) && IN(15) && MK_SINGLE;
;     ...
;       if (fused_) { xcd_barrier_arrive(bar); norm_router_table(args.in[20], args.in[21], (LAS float*)lds, tid_k); xcd_barrier_wait(bar); }
;     ...
;       if (!fused_) SEAM(14);
;       rt_ready = fused_; }
.LBB0_1259:
	v_readlane_b32 s4, v254, 12
	v_readlane_b32 s5, v254, 13
	s_cmp_lt_i32 s4, 16
	s_cselect_b64 s[4:5], -1, 0
	s_and_b64 s[6:7], s[4:5], s[6:7]
	v_cndmask_b32_e64 v1, 0, 1, s[6:7]
	v_cmp_ne_u32_e64 s[4:5], 1, v1
	s_andn2_b64 vcc, exec, s[6:7]
	s_nop 0
	v_writelane_b32 v254, s4, 57
	s_nop 1
	v_writelane_b32 v254, s5, 58
	s_cbranch_vccnz .LBB0_1281
	v_mov_b32_e32 v18, v0
	s_movk_i32 s4, 0x4000
	s_xor_b64 s[2:3], s[2:3], -1
	v_cmp_gt_i32_e32 vcc, s4, v18
	s_and_b64 s[4:5], s[2:3], vcc
	v_and_b32_e32 v1, 15, v18
	s_movk_i32 s2, 0x1010
	s_mov_b64 s[8:9], -1
	v_mad_u32_u24 v20, v1, s2, 0
	s_and_saveexec_b64 s[2:3], s[4:5]
	s_cbranch_execz .LBB0_1272
; #define LAS __attribute__((address_space(3)))
; __device__ __forceinline__ void norm_router_table(const float* g, const float* Wr, LAS float* WT, int tid) {
;     for (int idx = tid; idx < NE * DM; idx += NWAVES * 64) { const int e = idx & 15, d = idx >> 4; WT[e * WT_PITCH + ((d >> 3) & 3) * 256 + (d >> 5) * 8 + (d & 7)] = Wr[idx] * g[d]; }
; }
	v_readlane_b32 s4, v254, 40
	v_readlane_b32 s5, v254, 41
	v_readlane_b32 s6, v254, 38
	v_readlane_b32 s7, v254, 39
	v_lshlrev_b32_e32 v21, 2, v18
	v_lshrrev_b32_e32 v22, 4, v18
	v_lshlrev_b32_e32 v23, 2, v22
	v_lshrrev_b32_e32 v24, 3, v22
	v_and_b32_e32 v25, 7, v22
	v_lshl_add_u32 v24, v24, 10, v20
	v_lshl_add_u32 v24, v25, 2, v24
	global_load_dword v30, v21, s[4:5]
	global_load_dword v31, v21, s[4:5] offset:2048
	s_add_u32 s8, s4, 0x1000
	s_addc_u32 s9, s5, 0
	global_load_dword v32, v21, s[8:9]
	global_load_dword v33, v21, s[8:9] offset:2048
	s_add_u32 s8, s4, 0x2000
	s_addc_u32 s9, s5, 0
	global_load_dword v34, v21, s[8:9]
	global_load_dword v35, v21, s[8:9] offset:2048
	s_add_u32 s8, s4, 0x3000
	s_addc_u32 s9, s5, 0
	global_load_dword v36, v21, s[8:9]
	global_load_dword v37, v21, s[8:9] offset:2048
	s_add_u32 s8, s4, 0x4000
	s_addc_u32 s9, s5, 0
	global_load_dword v38, v21, s[8:9]
	global_load_dword v39, v21, s[8:9] offset:2048
	s_add_u32 s8, s4, 0x5000
	s_addc_u32 s9, s5, 0
	global_load_dword v40, v21, s[8:9]
	global_load_dword v41, v21, s[8:9] offset:2048
	s_add_u32 s8, s4, 0x6000
	s_addc_u32 s9, s5, 0
	global_load_dword v42, v21, s[8:9]
	global_load_dword v43, v21, s[8:9] offset:2048
	s_add_u32 s8, s4, 0x7000
	s_addc_u32 s9, s5, 0
	global_load_dword v44, v21, s[8:9]
	global_load_dword v45, v21, s[8:9] offset:2048
	s_add_u32 s8, s4, 0x8000
	s_addc_u32 s9, s5, 0
	global_load_dword v46, v21, s[8:9]
	global_load_dword v47, v21, s[8:9] offset:2048
	s_add_u32 s8, s4, 0x9000
	s_addc_u32 s9, s5, 0
	global_load_dword v48, v21, s[8:9]
	global_load_dword v49, v21, s[8:9] offset:2048
	s_add_u32 s8, s4, 0xa000
	s_addc_u32 s9, s5, 0
	global_load_dword v50, v21, s[8:9]
	global_load_dword v51, v21, s[8:9] offset:2048
	s_add_u32 s8, s4, 0xb000
	s_addc_u32 s9, s5, 0
	global_load_dword v52, v21, s[8:9]
	global_load_dword v53, v21, s[8:9] offset:2048
	s_add_u32 s8, s4, 0xc000
	s_addc_u32 s9, s5, 0
	global_load_dword v54, v21, s[8:9]
	global_load_dword v55, v21, s[8:9] offset:2048
	s_add_u32 s8, s4, 0xd000
	s_addc_u32 s9, s5, 0
	global_load_dword v56, v21, s[8:9]
	global_load_dword v57, v21, s[8:9] offset:2048
	s_add_u32 s8, s4, 0xe000
	s_addc_u32 s9, s5, 0
	global_load_dword v58, v21, s[8:9]
	global_load_dword v59, v21, s[8:9] offset:2048
	s_add_u32 s8, s4, 0xf000
	s_addc_u32 s9, s5, 0
	global_load_dword v60, v21, s[8:9]
	global_load_dword v61, v21, s[8:9] offset:2048
	global_load_dword v62, v23, s[6:7]
	global_load_dword v63, v23, s[6:7] offset:128
	global_load_dword v64, v23, s[6:7] offset:256
	global_load_dword v65, v23, s[6:7] offset:384
	global_load_dword v66, v23, s[6:7] offset:512
	global_load_dword v67, v23, s[6:7] offset:640
	global_load_dword v68, v23, s[6:7] offset:768
	global_load_dword v69, v23, s[6:7] offset:896
	global_load_dword v70, v23, s[6:7] offset:1024
	global_load_dword v71, v23, s[6:7] offset:1152
	global_load_dword v72, v23, s[6:7] offset:1280
	global_load_dword v73, v23, s[6:7] offset:1408
	global_load_dword v74, v23, s[6:7] offset:1536
	global_load_dword v75, v23, s[6:7] offset:1664
	global_load_dword v76, v23, s[6:7] offset:1792
	global_load_dword v77, v23, s[6:7] offset:1920
	global_load_dword v78, v23, s[6:7] offset:2048
	global_load_dword v79, v23, s[6:7] offset:2176
	global_load_dword v80, v23, s[6:7] offset:2304
	global_load_dword v81, v23, s[6:7] offset:2432
	global_load_dword v82, v23, s[6:7] offset:2560
	global_load_dword v83, v23, s[6:7] offset:2688
	global_load_dword v84, v23, s[6:7] offset:2816
	global_load_dword v85, v23, s[6:7] offset:2944
	global_load_dword v86, v23, s[6:7] offset:3072
	global_load_dword v87, v23, s[6:7] offset:3200
	global_load_dword v88, v23, s[6:7] offset:3328
	global_load_dword v89, v23, s[6:7] offset:3456
	global_load_dword v90, v23, s[6:7] offset:3584
	global_load_dword v91, v23, s[6:7] offset:3712
	global_load_dword v92, v23, s[6:7] offset:3840
	global_load_dword v93, v23, s[6:7] offset:3968
	s_waitcnt vmcnt(31)
	v_mul_f32_e32 v30, v30, v62
	ds_write_b32 v24, v30
	s_waitcnt vmcnt(30)
	v_mul_f32_e32 v31, v31, v63
	ds_write_b32 v24, v31 offset:32
	s_waitcnt vmcnt(29)
	v_mul_f32_e32 v32, v32, v64
	ds_write_b32 v24, v32 offset:64
	s_waitcnt vmcnt(28)
	v_mul_f32_e32 v33, v33, v65
	ds_write_b32 v24, v33 offset:96
	s_waitcnt vmcnt(27)
	v_mul_f32_e32 v34, v34, v66
	ds_write_b32 v24, v34 offset:128
	s_waitcnt vmcnt(26)
	v_mul_f32_e32 v35, v35, v67
	ds_write_b32 v24, v35 offset:160
	s_waitcnt vmcnt(25)
	v_mul_f32_e32 v36, v36, v68
	ds_write_b32 v24, v36 offset:192
	s_waitcnt vmcnt(24)
	v_mul_f32_e32 v37, v37, v69
	ds_write_b32 v24, v37 offset:224
	s_waitcnt vmcnt(23)
	v_mul_f32_e32 v38, v38, v70
	ds_write_b32 v24, v38 offset:256
	s_waitcnt vmcnt(22)
	v_mul_f32_e32 v39, v39, v71
	ds_write_b32 v24, v39 offset:288
	s_waitcnt vmcnt(21)
	v_mul_f32_e32 v40, v40, v72
	ds_write_b32 v24, v40 offset:320
	s_waitcnt vmcnt(20)
	v_mul_f32_e32 v41, v41, v73
	ds_write_b32 v24, v41 offset:352
	s_waitcnt vmcnt(19)
	v_mul_f32_e32 v42, v42, v74
	ds_write_b32 v24, v42 offset:384
	s_waitcnt vmcnt(18)
	v_mul_f32_e32 v43, v43, v75
	ds_write_b32 v24, v43 offset:416
	s_waitcnt vmcnt(17)
	v_mul_f32_e32 v44, v44, v76
	ds_write_b32 v24, v44 offset:448
	s_waitcnt vmcnt(16)
	v_mul_f32_e32 v45, v45, v77
	ds_write_b32 v24, v45 offset:480
	s_waitcnt vmcnt(15)
	v_mul_f32_e32 v46, v46, v78
	ds_write_b32 v24, v46 offset:512
	s_waitcnt vmcnt(14)
	v_mul_f32_e32 v47, v47, v79
	ds_write_b32 v24, v47 offset:544
	s_waitcnt vmcnt(13)
	v_mul_f32_e32 v48, v48, v80
	ds_write_b32 v24, v48 offset:576
	s_waitcnt vmcnt(12)
	v_mul_f32_e32 v49, v49, v81
	ds_write_b32 v24, v49 offset:608
	s_waitcnt vmcnt(11)
	v_mul_f32_e32 v50, v50, v82
	ds_write_b32 v24, v50 offset:640
	s_waitcnt vmcnt(10)
	v_mul_f32_e32 v51, v51, v83
	ds_write_b32 v24, v51 offset:672
	s_waitcnt vmcnt(9)
	v_mul_f32_e32 v52, v52, v84
	ds_write_b32 v24, v52 offset:704
	s_waitcnt vmcnt(8)
	v_mul_f32_e32 v53, v53, v85
	ds_write_b32 v24, v53 offset:736
	s_waitcnt vmcnt(7)
	v_mul_f32_e32 v54, v54, v86
	ds_write_b32 v24, v54 offset:768
	s_waitcnt vmcnt(6)
	v_mul_f32_e32 v55, v55, v87
	ds_write_b32 v24, v55 offset:800
	s_waitcnt vmcnt(5)
	v_mul_f32_e32 v56, v56, v88
	ds_write_b32 v24, v56 offset:832
	s_waitcnt vmcnt(4)
	v_mul_f32_e32 v57, v57, v89
	ds_write_b32 v24, v57 offset:864
	s_waitcnt vmcnt(3)
	v_mul_f32_e32 v58, v58, v90
	ds_write_b32 v24, v58 offset:896
	s_waitcnt vmcnt(2)
	v_mul_f32_e32 v59, v59, v91
	ds_write_b32 v24, v59 offset:928
	s_waitcnt vmcnt(1)
	v_mul_f32_e32 v60, v60, v92
	ds_write_b32 v24, v60 offset:960
	s_waitcnt vmcnt(0)
	v_mul_f32_e32 v61, v61, v93
	ds_write_b32 v24, v61 offset:992
